# GEMM2 epilogue (X += gate*acc): the 16 X row-piece loads issued together with the gate loads at the top of the epilogue (was load/wait/fma/store x16); plus router, combine, diff-combine load batching
# speedup vs baseline: 1.0215x; 1.0060x over previous
; __device__ __forceinline__ f32x4 ldx4(const bf16_t* q) { const u32x2 w = *(const u32x2*)q; f32x4 r; r.x = __uint_as_float(w.x << 16); r.y = __uint_as_float(w.x & 0xffff0000u); r.z = __uint_as_float(w.y << 16); r.w = __uint_as_float(w.y & 0xffff0000u); return r; }
; __device__ __forceinline__ void stx4(bf16_t* q, const f32x4 v) { u32x2 w; w.x = pk2(v.x, v.y); w.y = pk2(v.z, v.w); *(u32x2*)q = w; }
; __device__ __forceinline__ void ldx8(const bf16_t* q, f32x4& a, f32x4& b) { const u32x4 w = *(const u32x4*)q;
;   a.x = __uint_as_float(w.x << 16); a.y = __uint_as_float(w.x & 0xffff0000u); a.z = __uint_as_float(w.y << 16); a.w = __uint_as_float(w.y & 0xffff0000u);
;   b.x = __uint_as_float(w.z << 16); b.y = __uint_as_float(w.z & 0xffff0000u); b.z = __uint_as_float(w.w << 16); b.w = __uint_as_float(w.w & 0xffff0000u); }
;   __device__ __forceinline__ void operator()(const f32x4 (&acc)[2][2][4][2], const pg8::Unit& u, int wr, int wc, int fr, int fq) const {
;     const int row0 = rowbase + u.pm * 256 + wr * 64 + fr, col0 = u.pn * 256 + wc * 32 + 8 * fq;
;     const float* gp = modl + ((rowbase + u.pm * 256) < CTXL ? MODW : 0) + 2 * DM + col0;
;     f32x4 g[2][2];
; #pragma unroll
;     for (int bj = 0; bj < 2; ++bj) { g[bj][0] = *(const f32x4*)(gp + bj * 128); g[bj][1] = *(const f32x4*)(gp + bj * 128 + 4); }
; #pragma unroll
;     for (int ai = 0; ai < 2; ++ai)
; #pragma unroll
;       for (int m = 0; m < 4; ++m) { bf16_t* rowp = X + (size_t)(row0 + ai * 128 + m * 16) * DM + col0; float ss = 0.f;
; #pragma unroll
;         for (int bj = 0; bj < 2; ++bj) { f32x4 x0, x1; ldx8(rowp + bj * 128, x0, x1);
;           x0 += g[bj][0] * acc[ai][bj][m][0]; x1 += g[bj][1] * acc[ai][bj][m][1];
;           ss += x0.x * x0.x + x0.y * x0.y + x0.z * x0.z + x0.w * x0.w + x1.x * x1.x + x1.y * x1.y + x1.z * x1.z + x1.w * x1.w;
;           stx8(rowp + bj * 128, x0, x1); }
;         { auto rr = __builtin_amdgcn_permlane16_swap(__float_as_uint(ss), __float_as_uint(ss), false, false); ss = __uint_as_float(rr[0]) + __uint_as_float(rr[1]); }
;         { auto rr = __builtin_amdgcn_permlane32_swap(__float_as_uint(ss), __float_as_uint(ss), false, false); ss = __uint_as_float(rr[0]) + __uint_as_float(rr[1]); }
;         if (fq == 0) rss[(size_t)(row0 + ai * 128 + m * 16) * 32 + u.pn * 4 + wc] = ss; }
.LBB0_666:
	s_lshl_b32 s3, s60, 8
	s_add_i32 s3, s3, s92
	s_cmpk_lt_i32 s3, 0x100
	v_add_u32_e32 v162, s3, v165
	s_cselect_b32 s6, 0xc000, 0
	v_ashrrev_i32_e32 v163, 31, v162
	v_lshl_or_b32 v160, s38, 8, v167
	s_add_u32 s6, s72, s6
	v_lshlrev_b64 v[80:81], 12, v[162:163]
	v_ashrrev_i32_e32 v161, 31, v160
	v_lshl_add_u64 v[80:81], s[20:21], 0, v[80:81]
	s_addc_u32 s7, s73, 0
	v_lshl_add_u64 v[174:175], v[160:161], 1, v[80:81]
	v_lshl_add_u64 v[80:81], v[160:161], 2, s[6:7]
	s_mov_b64 s[6:7], 0x388000
	global_load_dwordx4 v[170:173], v[174:175], off
	v_lshl_add_u64 v[82:83], v[80:81], 0, s[6:7]
	s_mov_b32 s3, 0x388000
	v_add_co_u32_e32 v80, vcc, s3, v80
	global_load_dwordx4 v[98:101], v[82:83], off offset:16
	s_nop 0
	v_addc_co_u32_e32 v81, vcc, 0, v81, vcc
	global_load_dwordx4 v[102:105], v[80:81], off
	global_load_dwordx4 v[84:87], v[82:83], off offset:512
	s_nop 0
	global_load_dwordx4 v[80:83], v[82:83], off offset:528
	s_lshl_b32 s38, s38, 2
	s_ashr_i32 s39, s38, 31
	global_load_dwordx4 v[184:187], v[174:175], off offset:256
	s_mov_b64 s[30:31], 0x10000
	v_lshl_add_u64 v[182:183], v[174:175], 0, s[30:31]
	global_load_dwordx4 v[188:191], v[182:183], off
	global_load_dwordx4 v[192:195], v[182:183], off offset:256
	s_mov_b64 s[30:31], 0x20000
	v_lshl_add_u64 v[182:183], v[174:175], 0, s[30:31]
	global_load_dwordx4 v[196:199], v[182:183], off
	global_load_dwordx4 v[200:203], v[182:183], off offset:256
	s_mov_b64 s[30:31], 0x30000
	v_lshl_add_u64 v[182:183], v[174:175], 0, s[30:31]
	global_load_dwordx4 v[204:207], v[182:183], off
	global_load_dwordx4 v[208:211], v[182:183], off offset:256
	s_mov_b64 s[30:31], 0x80000
	v_lshl_add_u64 v[182:183], v[174:175], 0, s[30:31]
	global_load_dwordx4 v[212:215], v[182:183], off
	global_load_dwordx4 v[224:227], v[182:183], off offset:256
	s_mov_b64 s[30:31], 0x90000
	v_lshl_add_u64 v[182:183], v[174:175], 0, s[30:31]
	global_load_dwordx4 v[228:231], v[182:183], off
	global_load_dwordx4 v[232:235], v[182:183], off offset:256
	s_mov_b64 s[30:31], 0xa0000
	v_lshl_add_u64 v[182:183], v[174:175], 0, s[30:31]
	global_load_dwordx4 v[236:239], v[182:183], off
	global_load_dwordx4 v[240:243], v[182:183], off offset:256
	s_mov_b64 s[30:31], 0xb0000
	v_lshl_add_u64 v[182:183], v[174:175], 0, s[30:31]
	global_load_dwordx4 v[244:247], v[182:183], off
	global_load_dwordx4 v[248:251], v[182:183], off offset:256
	s_waitcnt vmcnt(0)
	v_lshlrev_b32_e32 v176, 16, v170
	v_and_b32_e32 v177, 0xffff0000, v170
	v_lshlrev_b32_e32 v170, 16, v171
	v_and_b32_e32 v171, 0xffff0000, v171
	v_lshlrev_b32_e32 v180, 16, v172
	v_and_b32_e32 v181, 0xffff0000, v172
	v_lshlrev_b32_e32 v172, 16, v173
	v_and_b32_e32 v173, 0xffff0000, v173
	v_pk_fma_f32 v[172:173], v[140:141], v[100:101], v[172:173]
	v_pk_fma_f32 v[180:181], v[138:139], v[98:99], v[180:181]
	v_pk_fma_f32 v[170:171], v[144:145], v[104:105], v[170:171]
	v_pk_fma_f32 v[176:177], v[142:143], v[102:103], v[176:177]
	s_nop 0
	v_cvt_pk_bf16_f32 v138, v176, v177
	v_cvt_pk_bf16_f32 v139, v170, v171
	v_cvt_pk_bf16_f32 v140, v180, v181
	v_cvt_pk_bf16_f32 v141, v172, v173
	v_mul_f32_e32 v169, v177, v177
	global_store_dwordx4 v[174:175], v[138:141], off
	v_fmac_f32_e32 v169, v176, v176
	v_fmac_f32_e32 v169, v170, v170
	v_fmac_f32_e32 v169, v171, v171
	v_fmac_f32_e32 v169, v180, v180
	v_fmac_f32_e32 v169, v181, v181
	v_fmac_f32_e32 v169, v172, v172
	v_fmac_f32_e32 v169, v173, v173
	v_lshlrev_b32_e32 v138, 16, v184
	v_and_b32_e32 v139, 0xffff0000, v184
	v_lshlrev_b32_e32 v140, 16, v185
	v_and_b32_e32 v141, 0xffff0000, v185
	v_lshlrev_b32_e32 v142, 16, v186
	v_and_b32_e32 v143, 0xffff0000, v186
	v_pk_fma_f32 v[134:135], v[134:135], v[84:85], v[138:139]
	v_pk_fma_f32 v[136:137], v[136:137], v[86:87], v[140:141]
	v_pk_fma_f32 v[140:141], v[130:131], v[80:81], v[142:143]
	v_mul_f32_e32 v142, v135, v135
	v_fmac_f32_e32 v142, v134, v134
	v_fmac_f32_e32 v142, v136, v136
	v_fmac_f32_e32 v142, v137, v137
	v_lshlrev_b32_e32 v144, 16, v187
	v_and_b32_e32 v145, 0xffff0000, v187
	v_fmac_f32_e32 v142, v140, v140
	v_pk_fma_f32 v[138:139], v[132:133], v[82:83], v[144:145]
	v_fmac_f32_e32 v142, v141, v141
	v_fmac_f32_e32 v142, v138, v138
	v_cvt_pk_bf16_f32 v130, v134, v135
	v_fmac_f32_e32 v142, v139, v139
	v_cvt_pk_bf16_f32 v131, v136, v137
	v_cvt_pk_bf16_f32 v132, v140, v141
	v_cvt_pk_bf16_f32 v133, v138, v139
	global_store_dwordx4 v[174:175], v[130:133], off offset:256
	s_nop 1
	v_add_f32_e32 v130, v169, v142
	v_mov_b32_e32 v131, v130
	s_nop 1
	v_permlane16_swap_b32_e32 v130, v131
	v_add_f32_e32 v130, v130, v131
	v_mov_b32_e32 v131, v130
	s_nop 1
	v_permlane32_swap_b32_e32 v130, v131
	s_and_saveexec_b64 s[6:7], s[40:41]
	s_cbranch_execz .LBB0_668
	v_lshlrev_b64 v[132:133], 7, v[162:163]
	v_lshl_add_u64 v[132:133], s[22:23], 0, v[132:133]
	v_lshl_add_u64 v[132:133], s[38:39], 2, v[132:133]
	s_lshl_b32 s64, s74, 2
	v_lshl_add_u64 v[132:133], v[132:133], 0, s[64:65]
	v_add_f32_e32 v130, v130, v131
	global_store_dword v[132:133], v130, off
; __device__ __forceinline__ void stx8(bf16_t* q, const f32x4 a, const f32x4 b) { u32x4 w; w.x = pk2(a.x, a.y); w.y = pk2(a.z, a.w); w.z = pk2(b.x, b.y); w.w = pk2(b.z, b.w); *(u32x4*)q = w; }
;   __device__ __forceinline__ void operator()(const f32x4 (&acc)[2][2][4][2], const pg8::Unit& u, int wr, int wc, int fr, int fq) const {
;     ...
;       for (int m = 0; m < 4; ++m) { bf16_t* rowp = X + (size_t)(row0 + ai * 128 + m * 16) * DM + col0; float ss = 0.f;
; #pragma unroll
;         for (int bj = 0; bj < 2; ++bj) { f32x4 x0, x1; ldx8(rowp + bj * 128, x0, x1);
;           x0 += g[bj][0] * acc[ai][bj][m][0]; x1 += g[bj][1] * acc[ai][bj][m][1];
;           ss += x0.x * x0.x + x0.y * x0.y + x0.z * x0.z + x0.w * x0.w + x1.x * x1.x + x1.y * x1.y + x1.z * x1.z + x1.w * x1.w;
;           stx8(rowp + bj * 128, x0, x1); }
;         { auto rr = __builtin_amdgcn_permlane16_swap(__float_as_uint(ss), __float_as_uint(ss), false, false); ss = __uint_as_float(rr[0]) + __uint_as_float(rr[1]); }
;         { auto rr = __builtin_amdgcn_permlane32_swap(__float_as_uint(ss), __float_as_uint(ss), false, false); ss = __uint_as_float(rr[0]) + __uint_as_float(rr[1]); }
;         if (fq == 0) rss[(size_t)(row0 + ai * 128 + m * 16) * 32 + u.pn * 4 + wc] = ss; }
.LBB0_668:
	s_or_b64 exec, exec, s[6:7]
	v_or_b32_e32 v130, 16, v162
	v_ashrrev_i32_e32 v131, 31, v130
	v_lshlrev_b64 v[132:133], 12, v[130:131]
	v_lshl_add_u64 v[132:133], s[20:21], 0, v[132:133]
	v_lshl_add_u64 v[136:137], v[160:161], 1, v[132:133]
	v_lshlrev_b32_e32 v138, 16, v188
	v_and_b32_e32 v139, 0xffff0000, v188
	v_lshlrev_b32_e32 v132, 16, v189
	v_and_b32_e32 v133, 0xffff0000, v189
	v_lshlrev_b32_e32 v140, 16, v190
	v_and_b32_e32 v141, 0xffff0000, v190
	v_lshlrev_b32_e32 v134, 16, v191
	v_and_b32_e32 v135, 0xffff0000, v191
	v_pk_fma_f32 v[132:133], v[128:129], v[104:105], v[132:133]
	v_pk_fma_f32 v[138:139], v[126:127], v[102:103], v[138:139]
	v_pk_fma_f32 v[134:135], v[124:125], v[100:101], v[134:135]
	v_pk_fma_f32 v[140:141], v[122:123], v[98:99], v[140:141]
	v_cvt_pk_bf16_f32 v122, v138, v139
	v_cvt_pk_bf16_f32 v123, v132, v133
	v_mul_f32_e32 v139, v139, v139
	v_cvt_pk_bf16_f32 v124, v140, v141
	v_cvt_pk_bf16_f32 v125, v134, v135
	v_fmac_f32_e32 v139, v138, v138
	global_store_dwordx4 v[136:137], v[122:125], off
	v_fmac_f32_e32 v139, v132, v132
	v_fmac_f32_e32 v139, v133, v133
	v_fmac_f32_e32 v139, v140, v140
	v_fmac_f32_e32 v139, v141, v141
	v_fmac_f32_e32 v139, v134, v134
	v_fmac_f32_e32 v139, v135, v135
	v_lshlrev_b32_e32 v122, 16, v192
	v_and_b32_e32 v123, 0xffff0000, v192
	v_lshlrev_b32_e32 v124, 16, v193
	v_and_b32_e32 v125, 0xffff0000, v193
	v_lshlrev_b32_e32 v126, 16, v194
	v_and_b32_e32 v127, 0xffff0000, v194
	v_pk_fma_f32 v[118:119], v[118:119], v[84:85], v[122:123]
	v_pk_fma_f32 v[120:121], v[120:121], v[86:87], v[124:125]
	v_pk_fma_f32 v[124:125], v[114:115], v[80:81], v[126:127]
	v_mul_f32_e32 v126, v119, v119
	v_fmac_f32_e32 v126, v118, v118
	v_fmac_f32_e32 v126, v120, v120
	v_fmac_f32_e32 v126, v121, v121
	v_lshlrev_b32_e32 v128, 16, v195
	v_and_b32_e32 v129, 0xffff0000, v195
	v_fmac_f32_e32 v126, v124, v124
	v_pk_fma_f32 v[122:123], v[116:117], v[82:83], v[128:129]
	v_fmac_f32_e32 v126, v125, v125
	v_fmac_f32_e32 v126, v122, v122
	v_cvt_pk_bf16_f32 v114, v118, v119
	v_fmac_f32_e32 v126, v123, v123
	v_cvt_pk_bf16_f32 v115, v120, v121
	v_cvt_pk_bf16_f32 v116, v124, v125
	v_cvt_pk_bf16_f32 v117, v122, v123
	global_store_dwordx4 v[136:137], v[114:117], off offset:256
	s_nop 1
	v_add_f32_e32 v114, v139, v126
	v_mov_b32_e32 v115, v114
	s_nop 1
	v_permlane16_swap_b32_e32 v114, v115
	v_add_f32_e32 v114, v114, v115
	v_mov_b32_e32 v115, v114
	s_nop 1
	v_permlane32_swap_b32_e32 v114, v115
	s_and_saveexec_b64 s[6:7], s[40:41]
	s_cbranch_execz .LBB0_670
	v_lshlrev_b64 v[116:117], 7, v[130:131]
	v_lshl_add_u64 v[116:117], s[22:23], 0, v[116:117]
	v_lshl_add_u64 v[116:117], s[38:39], 2, v[116:117]
	s_lshl_b32 s64, s74, 2
	v_lshl_add_u64 v[116:117], v[116:117], 0, s[64:65]
	v_add_f32_e32 v114, v114, v115
	global_store_dword v[116:117], v114, off
.LBB0_670:
	s_or_b64 exec, exec, s[6:7]
	v_or_b32_e32 v114, 32, v162
	v_ashrrev_i32_e32 v115, 31, v114
	v_lshlrev_b64 v[116:117], 12, v[114:115]
	v_lshl_add_u64 v[116:117], s[20:21], 0, v[116:117]
	v_lshl_add_u64 v[120:121], v[160:161], 1, v[116:117]
	v_lshlrev_b32_e32 v122, 16, v196
	v_and_b32_e32 v123, 0xffff0000, v196
	v_lshlrev_b32_e32 v116, 16, v197
	v_and_b32_e32 v117, 0xffff0000, v197
	v_lshlrev_b32_e32 v124, 16, v198
	v_and_b32_e32 v125, 0xffff0000, v198
	v_lshlrev_b32_e32 v118, 16, v199
	v_and_b32_e32 v119, 0xffff0000, v199
	v_pk_fma_f32 v[116:117], v[112:113], v[104:105], v[116:117]
	v_pk_fma_f32 v[122:123], v[110:111], v[102:103], v[122:123]
	v_pk_fma_f32 v[118:119], v[108:109], v[100:101], v[118:119]
	v_pk_fma_f32 v[124:125], v[106:107], v[98:99], v[124:125]
	v_cvt_pk_bf16_f32 v106, v122, v123
	v_cvt_pk_bf16_f32 v107, v116, v117
	v_mul_f32_e32 v123, v123, v123
	v_cvt_pk_bf16_f32 v108, v124, v125
	v_cvt_pk_bf16_f32 v109, v118, v119
	v_fmac_f32_e32 v123, v122, v122
	global_store_dwordx4 v[120:121], v[106:109], off
	v_fmac_f32_e32 v123, v116, v116
	v_fmac_f32_e32 v123, v117, v117
	v_fmac_f32_e32 v123, v124, v124
	v_fmac_f32_e32 v123, v125, v125
	v_fmac_f32_e32 v123, v118, v118
	v_fmac_f32_e32 v123, v119, v119
	v_lshlrev_b32_e32 v106, 16, v200
	v_and_b32_e32 v107, 0xffff0000, v200
	v_lshlrev_b32_e32 v108, 16, v201
	v_and_b32_e32 v109, 0xffff0000, v201
	v_lshlrev_b32_e32 v110, 16, v202
	v_and_b32_e32 v111, 0xffff0000, v202
	v_pk_fma_f32 v[92:93], v[92:93], v[84:85], v[106:107]
	v_pk_fma_f32 v[94:95], v[94:95], v[86:87], v[108:109]
	v_pk_fma_f32 v[108:109], v[88:89], v[80:81], v[110:111]
	v_mul_f32_e32 v110, v93, v93
	v_fmac_f32_e32 v110, v92, v92
	v_fmac_f32_e32 v110, v94, v94
	v_fmac_f32_e32 v110, v95, v95
	v_lshlrev_b32_e32 v112, 16, v203
	v_and_b32_e32 v113, 0xffff0000, v203
	v_fmac_f32_e32 v110, v108, v108
	v_pk_fma_f32 v[106:107], v[90:91], v[82:83], v[112:113]
	v_fmac_f32_e32 v110, v109, v109
	v_fmac_f32_e32 v110, v106, v106
	v_cvt_pk_bf16_f32 v88, v92, v93
	v_fmac_f32_e32 v110, v107, v107
	v_cvt_pk_bf16_f32 v89, v94, v95
	v_cvt_pk_bf16_f32 v90, v108, v109
	v_cvt_pk_bf16_f32 v91, v106, v107
	global_store_dwordx4 v[120:121], v[88:91], off offset:256
	s_nop 1
	v_add_f32_e32 v88, v123, v110
	v_mov_b32_e32 v89, v88
	s_nop 1
	v_permlane16_swap_b32_e32 v88, v89
	v_add_f32_e32 v88, v88, v89
	v_mov_b32_e32 v89, v88
	s_nop 1
	v_permlane32_swap_b32_e32 v88, v89
	s_and_saveexec_b64 s[6:7], s[40:41]
	s_cbranch_execz .LBB0_672
	v_lshlrev_b64 v[90:91], 7, v[114:115]
	v_lshl_add_u64 v[90:91], s[22:23], 0, v[90:91]
	v_lshl_add_u64 v[90:91], s[38:39], 2, v[90:91]
	s_lshl_b32 s64, s74, 2
	v_lshl_add_u64 v[90:91], v[90:91], 0, s[64:65]
	v_add_f32_e32 v88, v88, v89
	global_store_dword v[90:91], v88, off
; __device__ __forceinline__ void stx8(bf16_t* q, const f32x4 a, const f32x4 b) { u32x4 w; w.x = pk2(a.x, a.y); w.y = pk2(a.z, a.w); w.z = pk2(b.x, b.y); w.w = pk2(b.z, b.w); *(u32x4*)q = w; }
;   __device__ __forceinline__ void operator()(const f32x4 (&acc)[2][2][4][2], const pg8::Unit& u, int wr, int wc, int fr, int fq) const {
;     ...
;       for (int m = 0; m < 4; ++m) { bf16_t* rowp = X + (size_t)(row0 + ai * 128 + m * 16) * DM + col0; float ss = 0.f;
; #pragma unroll
;         for (int bj = 0; bj < 2; ++bj) { f32x4 x0, x1; ldx8(rowp + bj * 128, x0, x1);
;           x0 += g[bj][0] * acc[ai][bj][m][0]; x1 += g[bj][1] * acc[ai][bj][m][1];
;           ss += x0.x * x0.x + x0.y * x0.y + x0.z * x0.z + x0.w * x0.w + x1.x * x1.x + x1.y * x1.y + x1.z * x1.z + x1.w * x1.w;
;           stx8(rowp + bj * 128, x0, x1); }
;         { auto rr = __builtin_amdgcn_permlane16_swap(__float_as_uint(ss), __float_as_uint(ss), false, false); ss = __uint_as_float(rr[0]) + __uint_as_float(rr[1]); }
;         { auto rr = __builtin_amdgcn_permlane32_swap(__float_as_uint(ss), __float_as_uint(ss), false, false); ss = __uint_as_float(rr[0]) + __uint_as_float(rr[1]); }
;         if (fq == 0) rss[(size_t)(row0 + ai * 128 + m * 16) * 32 + u.pn * 4 + wc] = ss; }
.LBB0_672:
	s_or_b64 exec, exec, s[6:7]
	v_or_b32_e32 v88, 48, v162
	v_ashrrev_i32_e32 v89, 31, v88
	v_lshlrev_b64 v[90:91], 12, v[88:89]
	v_lshl_add_u64 v[90:91], s[20:21], 0, v[90:91]
	v_lshl_add_u64 v[94:95], v[160:161], 1, v[90:91]
	v_lshlrev_b32_e32 v106, 16, v204
	v_and_b32_e32 v107, 0xffff0000, v204
	v_lshlrev_b32_e32 v90, 16, v205
	v_and_b32_e32 v91, 0xffff0000, v205
	v_lshlrev_b32_e32 v108, 16, v206
	v_and_b32_e32 v109, 0xffff0000, v206
	v_lshlrev_b32_e32 v92, 16, v207
	v_and_b32_e32 v93, 0xffff0000, v207
	v_pk_fma_f32 v[90:91], v[78:79], v[104:105], v[90:91]
	v_pk_fma_f32 v[106:107], v[76:77], v[102:103], v[106:107]
	v_pk_fma_f32 v[92:93], v[74:75], v[100:101], v[92:93]
	v_pk_fma_f32 v[108:109], v[72:73], v[98:99], v[108:109]
	v_cvt_pk_bf16_f32 v72, v106, v107
	v_cvt_pk_bf16_f32 v73, v90, v91
	v_mul_f32_e32 v107, v107, v107
	v_cvt_pk_bf16_f32 v74, v108, v109
	v_cvt_pk_bf16_f32 v75, v92, v93
	v_fmac_f32_e32 v107, v106, v106
	global_store_dwordx4 v[94:95], v[72:75], off
	v_fmac_f32_e32 v107, v90, v90
	v_fmac_f32_e32 v107, v91, v91
	v_fmac_f32_e32 v107, v108, v108
	v_fmac_f32_e32 v107, v109, v109
	v_fmac_f32_e32 v107, v92, v92
	v_fmac_f32_e32 v107, v93, v93
	v_lshlrev_b32_e32 v72, 16, v208
	v_and_b32_e32 v73, 0xffff0000, v208
	v_lshlrev_b32_e32 v74, 16, v209
	v_and_b32_e32 v75, 0xffff0000, v209
	v_lshlrev_b32_e32 v76, 16, v210
	v_and_b32_e32 v77, 0xffff0000, v210
	v_pk_fma_f32 v[68:69], v[68:69], v[84:85], v[72:73]
	v_pk_fma_f32 v[70:71], v[70:71], v[86:87], v[74:75]
	v_pk_fma_f32 v[74:75], v[64:65], v[80:81], v[76:77]
	v_mul_f32_e32 v76, v69, v69
	v_fmac_f32_e32 v76, v68, v68
	v_fmac_f32_e32 v76, v70, v70
	v_fmac_f32_e32 v76, v71, v71
	v_lshlrev_b32_e32 v78, 16, v211
	v_and_b32_e32 v79, 0xffff0000, v211
	v_fmac_f32_e32 v76, v74, v74
	v_pk_fma_f32 v[72:73], v[66:67], v[82:83], v[78:79]
	v_fmac_f32_e32 v76, v75, v75
	v_fmac_f32_e32 v76, v72, v72
	v_cvt_pk_bf16_f32 v64, v68, v69
	v_fmac_f32_e32 v76, v73, v73
	v_cvt_pk_bf16_f32 v65, v70, v71
	v_cvt_pk_bf16_f32 v66, v74, v75
	v_cvt_pk_bf16_f32 v67, v72, v73
	global_store_dwordx4 v[94:95], v[64:67], off offset:256
	s_nop 1
	v_add_f32_e32 v64, v107, v76
	v_mov_b32_e32 v65, v64
	s_nop 1
	v_permlane16_swap_b32_e32 v64, v65
	v_add_f32_e32 v64, v64, v65
	v_mov_b32_e32 v65, v64
	s_nop 1
	v_permlane32_swap_b32_e32 v64, v65
	s_and_saveexec_b64 s[6:7], s[40:41]
	s_cbranch_execz .LBB0_674
	v_lshlrev_b64 v[66:67], 7, v[88:89]
	v_lshl_add_u64 v[66:67], s[22:23], 0, v[66:67]
	v_lshl_add_u64 v[66:67], s[38:39], 2, v[66:67]
	s_lshl_b32 s64, s74, 2
	v_lshl_add_u64 v[66:67], v[66:67], 0, s[64:65]
	v_add_f32_e32 v64, v64, v65
	global_store_dword v[66:67], v64, off
.LBB0_674:
	s_or_b64 exec, exec, s[6:7]
	v_add_u32_e32 v64, 0x80, v162
	v_ashrrev_i32_e32 v65, 31, v64
	v_lshlrev_b64 v[66:67], 12, v[64:65]
	v_lshl_add_u64 v[66:67], s[20:21], 0, v[66:67]
	v_lshl_add_u64 v[70:71], v[160:161], 1, v[66:67]
	v_lshlrev_b32_e32 v72, 16, v212
	v_and_b32_e32 v73, 0xffff0000, v212
	v_lshlrev_b32_e32 v66, 16, v213
	v_and_b32_e32 v67, 0xffff0000, v213
	v_lshlrev_b32_e32 v74, 16, v214
	v_and_b32_e32 v75, 0xffff0000, v214
	v_lshlrev_b32_e32 v68, 16, v215
	v_and_b32_e32 v69, 0xffff0000, v215
	v_pk_fma_f32 v[66:67], v[62:63], v[104:105], v[66:67]
	v_pk_fma_f32 v[72:73], v[60:61], v[102:103], v[72:73]
	v_pk_fma_f32 v[68:69], v[58:59], v[100:101], v[68:69]
	v_pk_fma_f32 v[74:75], v[56:57], v[98:99], v[74:75]
	v_cvt_pk_bf16_f32 v56, v72, v73
	v_cvt_pk_bf16_f32 v57, v66, v67
	v_mul_f32_e32 v73, v73, v73
	v_cvt_pk_bf16_f32 v58, v74, v75
	v_cvt_pk_bf16_f32 v59, v68, v69
	v_fmac_f32_e32 v73, v72, v72
	global_store_dwordx4 v[70:71], v[56:59], off
	v_fmac_f32_e32 v73, v66, v66
	v_fmac_f32_e32 v73, v67, v67
	v_fmac_f32_e32 v73, v74, v74
	v_fmac_f32_e32 v73, v75, v75
	v_fmac_f32_e32 v73, v68, v68
	v_fmac_f32_e32 v73, v69, v69
	v_lshlrev_b32_e32 v56, 16, v224
	v_and_b32_e32 v57, 0xffff0000, v224
	v_lshlrev_b32_e32 v58, 16, v225
	v_and_b32_e32 v59, 0xffff0000, v225
	v_lshlrev_b32_e32 v60, 16, v226
	v_and_b32_e32 v61, 0xffff0000, v226
	v_pk_fma_f32 v[52:53], v[52:53], v[84:85], v[56:57]
	v_pk_fma_f32 v[54:55], v[54:55], v[86:87], v[58:59]
	v_pk_fma_f32 v[58:59], v[48:49], v[80:81], v[60:61]
	v_mul_f32_e32 v60, v53, v53
	v_fmac_f32_e32 v60, v52, v52
	v_fmac_f32_e32 v60, v54, v54
	v_fmac_f32_e32 v60, v55, v55
	v_lshlrev_b32_e32 v62, 16, v227
	v_and_b32_e32 v63, 0xffff0000, v227
	v_fmac_f32_e32 v60, v58, v58
	v_pk_fma_f32 v[56:57], v[50:51], v[82:83], v[62:63]
	v_fmac_f32_e32 v60, v59, v59
	v_fmac_f32_e32 v60, v56, v56
	v_cvt_pk_bf16_f32 v48, v52, v53
	v_fmac_f32_e32 v60, v57, v57
	v_cvt_pk_bf16_f32 v49, v54, v55
	v_cvt_pk_bf16_f32 v50, v58, v59
	v_cvt_pk_bf16_f32 v51, v56, v57
	global_store_dwordx4 v[70:71], v[48:51], off offset:256
	s_nop 1
	v_add_f32_e32 v48, v73, v60
	v_mov_b32_e32 v49, v48
	s_nop 1
	v_permlane16_swap_b32_e32 v48, v49
	v_add_f32_e32 v48, v48, v49
	v_mov_b32_e32 v49, v48
	s_nop 1
	v_permlane32_swap_b32_e32 v48, v49
	s_and_saveexec_b64 s[6:7], s[40:41]
	s_cbranch_execz .LBB0_676
	v_lshlrev_b64 v[50:51], 7, v[64:65]
	v_lshl_add_u64 v[50:51], s[22:23], 0, v[50:51]
	v_lshl_add_u64 v[50:51], s[38:39], 2, v[50:51]
	s_lshl_b32 s64, s74, 2
	v_lshl_add_u64 v[50:51], v[50:51], 0, s[64:65]
	v_add_f32_e32 v48, v48, v49
	global_store_dword v[50:51], v48, off
; __device__ __forceinline__ void stx8(bf16_t* q, const f32x4 a, const f32x4 b) { u32x4 w; w.x = pk2(a.x, a.y); w.y = pk2(a.z, a.w); w.z = pk2(b.x, b.y); w.w = pk2(b.z, b.w); *(u32x4*)q = w; }
;   __device__ __forceinline__ void operator()(const f32x4 (&acc)[2][2][4][2], const pg8::Unit& u, int wr, int wc, int fr, int fq) const {
;     ...
;       for (int m = 0; m < 4; ++m) { bf16_t* rowp = X + (size_t)(row0 + ai * 128 + m * 16) * DM + col0; float ss = 0.f;
; #pragma unroll
;         for (int bj = 0; bj < 2; ++bj) { f32x4 x0, x1; ldx8(rowp + bj * 128, x0, x1);
;           x0 += g[bj][0] * acc[ai][bj][m][0]; x1 += g[bj][1] * acc[ai][bj][m][1];
;           ss += x0.x * x0.x + x0.y * x0.y + x0.z * x0.z + x0.w * x0.w + x1.x * x1.x + x1.y * x1.y + x1.z * x1.z + x1.w * x1.w;
;           stx8(rowp + bj * 128, x0, x1); }
;         { auto rr = __builtin_amdgcn_permlane16_swap(__float_as_uint(ss), __float_as_uint(ss), false, false); ss = __uint_as_float(rr[0]) + __uint_as_float(rr[1]); }
;         { auto rr = __builtin_amdgcn_permlane32_swap(__float_as_uint(ss), __float_as_uint(ss), false, false); ss = __uint_as_float(rr[0]) + __uint_as_float(rr[1]); }
;         if (fq == 0) rss[(size_t)(row0 + ai * 128 + m * 16) * 32 + u.pn * 4 + wc] = ss; }
.LBB0_676:
	s_or_b64 exec, exec, s[6:7]
	v_add_u32_e32 v48, 0x90, v162
	v_ashrrev_i32_e32 v49, 31, v48
	v_lshlrev_b64 v[50:51], 12, v[48:49]
	v_lshl_add_u64 v[50:51], s[20:21], 0, v[50:51]
	v_lshl_add_u64 v[54:55], v[160:161], 1, v[50:51]
	v_lshlrev_b32_e32 v56, 16, v228
	v_and_b32_e32 v57, 0xffff0000, v228
	v_lshlrev_b32_e32 v50, 16, v229
	v_and_b32_e32 v51, 0xffff0000, v229
	v_lshlrev_b32_e32 v58, 16, v230
	v_and_b32_e32 v59, 0xffff0000, v230
	v_lshlrev_b32_e32 v52, 16, v231
	v_and_b32_e32 v53, 0xffff0000, v231
	v_pk_fma_f32 v[50:51], v[46:47], v[104:105], v[50:51]
	v_pk_fma_f32 v[56:57], v[44:45], v[102:103], v[56:57]
	v_pk_fma_f32 v[52:53], v[42:43], v[100:101], v[52:53]
	v_pk_fma_f32 v[58:59], v[40:41], v[98:99], v[58:59]
	v_cvt_pk_bf16_f32 v40, v56, v57
	v_cvt_pk_bf16_f32 v41, v50, v51
	v_mul_f32_e32 v57, v57, v57
	v_cvt_pk_bf16_f32 v42, v58, v59
	v_cvt_pk_bf16_f32 v43, v52, v53
	v_fmac_f32_e32 v57, v56, v56
	global_store_dwordx4 v[54:55], v[40:43], off
	v_fmac_f32_e32 v57, v50, v50
	v_fmac_f32_e32 v57, v51, v51
	v_fmac_f32_e32 v57, v58, v58
	v_fmac_f32_e32 v57, v59, v59
	v_fmac_f32_e32 v57, v52, v52
	v_fmac_f32_e32 v57, v53, v53
	v_lshlrev_b32_e32 v40, 16, v232
	v_and_b32_e32 v41, 0xffff0000, v232
	v_lshlrev_b32_e32 v42, 16, v233
	v_and_b32_e32 v43, 0xffff0000, v233
	v_lshlrev_b32_e32 v44, 16, v234
	v_and_b32_e32 v45, 0xffff0000, v234
	v_pk_fma_f32 v[36:37], v[36:37], v[84:85], v[40:41]
	v_pk_fma_f32 v[38:39], v[38:39], v[86:87], v[42:43]
	v_pk_fma_f32 v[42:43], v[32:33], v[80:81], v[44:45]
	v_mul_f32_e32 v44, v37, v37
	v_fmac_f32_e32 v44, v36, v36
	v_fmac_f32_e32 v44, v38, v38
	v_fmac_f32_e32 v44, v39, v39
	v_lshlrev_b32_e32 v46, 16, v235
	v_and_b32_e32 v47, 0xffff0000, v235
	v_fmac_f32_e32 v44, v42, v42
	v_pk_fma_f32 v[40:41], v[34:35], v[82:83], v[46:47]
	v_fmac_f32_e32 v44, v43, v43
	v_fmac_f32_e32 v44, v40, v40
	v_cvt_pk_bf16_f32 v32, v36, v37
	v_fmac_f32_e32 v44, v41, v41
	v_cvt_pk_bf16_f32 v33, v38, v39
	v_cvt_pk_bf16_f32 v34, v42, v43
	v_cvt_pk_bf16_f32 v35, v40, v41
	global_store_dwordx4 v[54:55], v[32:35], off offset:256
	s_nop 1
	v_add_f32_e32 v32, v57, v44
	v_mov_b32_e32 v33, v32
	s_nop 1
	v_permlane16_swap_b32_e32 v32, v33
	v_add_f32_e32 v32, v32, v33
	v_mov_b32_e32 v33, v32
	s_nop 1
	v_permlane32_swap_b32_e32 v32, v33
	s_and_saveexec_b64 s[6:7], s[40:41]
	s_cbranch_execz .LBB0_678
	v_lshlrev_b64 v[34:35], 7, v[48:49]
	v_lshl_add_u64 v[34:35], s[22:23], 0, v[34:35]
	v_lshl_add_u64 v[34:35], s[38:39], 2, v[34:35]
	s_lshl_b32 s64, s74, 2
	v_lshl_add_u64 v[34:35], v[34:35], 0, s[64:65]
	v_add_f32_e32 v32, v32, v33
	global_store_dword v[34:35], v32, off
; __device__ __forceinline__ void stx8(bf16_t* q, const f32x4 a, const f32x4 b) { u32x4 w; w.x = pk2(a.x, a.y); w.y = pk2(a.z, a.w); w.z = pk2(b.x, b.y); w.w = pk2(b.z, b.w); *(u32x4*)q = w; }
;   __device__ __forceinline__ void operator()(const f32x4 (&acc)[2][2][4][2], const pg8::Unit& u, int wr, int wc, int fr, int fq) const {
;     ...
;       for (int m = 0; m < 4; ++m) { bf16_t* rowp = X + (size_t)(row0 + ai * 128 + m * 16) * DM + col0; float ss = 0.f;
; #pragma unroll
;         for (int bj = 0; bj < 2; ++bj) { f32x4 x0, x1; ldx8(rowp + bj * 128, x0, x1);
;           x0 += g[bj][0] * acc[ai][bj][m][0]; x1 += g[bj][1] * acc[ai][bj][m][1];
;           ss += x0.x * x0.x + x0.y * x0.y + x0.z * x0.z + x0.w * x0.w + x1.x * x1.x + x1.y * x1.y + x1.z * x1.z + x1.w * x1.w;
;           stx8(rowp + bj * 128, x0, x1); }
;         { auto rr = __builtin_amdgcn_permlane16_swap(__float_as_uint(ss), __float_as_uint(ss), false, false); ss = __uint_as_float(rr[0]) + __uint_as_float(rr[1]); }
;         { auto rr = __builtin_amdgcn_permlane32_swap(__float_as_uint(ss), __float_as_uint(ss), false, false); ss = __uint_as_float(rr[0]) + __uint_as_float(rr[1]); }
;         if (fq == 0) rss[(size_t)(row0 + ai * 128 + m * 16) * 32 + u.pn * 4 + wc] = ss; }
.LBB0_678:
	s_or_b64 exec, exec, s[6:7]
	v_add_u32_e32 v32, 0xa0, v162
	v_ashrrev_i32_e32 v33, 31, v32
	v_lshlrev_b64 v[34:35], 12, v[32:33]
	v_lshl_add_u64 v[34:35], s[20:21], 0, v[34:35]
	v_lshl_add_u64 v[38:39], v[160:161], 1, v[34:35]
	v_lshlrev_b32_e32 v40, 16, v236
	v_and_b32_e32 v41, 0xffff0000, v236
	v_lshlrev_b32_e32 v34, 16, v237
	v_and_b32_e32 v35, 0xffff0000, v237
	v_lshlrev_b32_e32 v42, 16, v238
	v_and_b32_e32 v43, 0xffff0000, v238
	v_lshlrev_b32_e32 v36, 16, v239
	v_and_b32_e32 v37, 0xffff0000, v239
	v_pk_fma_f32 v[34:35], v[22:23], v[104:105], v[34:35]
	v_pk_fma_f32 v[40:41], v[20:21], v[102:103], v[40:41]
	v_pk_fma_f32 v[36:37], v[18:19], v[100:101], v[36:37]
	v_pk_fma_f32 v[42:43], v[16:17], v[98:99], v[42:43]
	v_cvt_pk_bf16_f32 v16, v40, v41
	v_cvt_pk_bf16_f32 v17, v34, v35
	v_mul_f32_e32 v41, v41, v41
	v_cvt_pk_bf16_f32 v18, v42, v43
	v_cvt_pk_bf16_f32 v19, v36, v37
	v_fmac_f32_e32 v41, v40, v40
	global_store_dwordx4 v[38:39], v[16:19], off
	v_fmac_f32_e32 v41, v34, v34
	v_fmac_f32_e32 v41, v35, v35
	v_fmac_f32_e32 v41, v42, v42
	v_fmac_f32_e32 v41, v43, v43
	v_fmac_f32_e32 v41, v36, v36
	v_fmac_f32_e32 v41, v37, v37
	v_lshlrev_b32_e32 v16, 16, v240
	v_and_b32_e32 v17, 0xffff0000, v240
	v_lshlrev_b32_e32 v18, 16, v241
	v_and_b32_e32 v19, 0xffff0000, v241
	v_lshlrev_b32_e32 v20, 16, v242
	v_and_b32_e32 v21, 0xffff0000, v242
	v_pk_fma_f32 v[28:29], v[28:29], v[84:85], v[16:17]
	v_pk_fma_f32 v[20:21], v[24:25], v[80:81], v[20:21]
	v_mul_f32_e32 v24, v29, v29
	v_pk_fma_f32 v[30:31], v[30:31], v[86:87], v[18:19]
	v_fmac_f32_e32 v24, v28, v28
	v_fmac_f32_e32 v24, v30, v30
	v_fmac_f32_e32 v24, v31, v31
	v_lshlrev_b32_e32 v22, 16, v243
	v_and_b32_e32 v23, 0xffff0000, v243
	v_fmac_f32_e32 v24, v20, v20
	v_pk_fma_f32 v[22:23], v[26:27], v[82:83], v[22:23]
	v_fmac_f32_e32 v24, v21, v21
	v_fmac_f32_e32 v24, v22, v22
	v_cvt_pk_bf16_f32 v16, v28, v29
	v_fmac_f32_e32 v24, v23, v23
	v_cvt_pk_bf16_f32 v17, v30, v31
	v_cvt_pk_bf16_f32 v18, v20, v21
	v_cvt_pk_bf16_f32 v19, v22, v23
	global_store_dwordx4 v[38:39], v[16:19], off offset:256
	s_nop 1
	v_add_f32_e32 v16, v41, v24
	v_mov_b32_e32 v17, v16
	s_nop 1
	v_permlane16_swap_b32_e32 v16, v17
	v_add_f32_e32 v16, v16, v17
	v_mov_b32_e32 v17, v16
	s_nop 1
	v_permlane32_swap_b32_e32 v16, v17
	s_and_saveexec_b64 s[6:7], s[40:41]
	s_cbranch_execz .LBB0_680
	v_lshlrev_b64 v[18:19], 7, v[32:33]
	v_lshl_add_u64 v[18:19], s[22:23], 0, v[18:19]
	v_lshl_add_u64 v[18:19], s[38:39], 2, v[18:19]
	s_lshl_b32 s64, s74, 2
	v_lshl_add_u64 v[18:19], v[18:19], 0, s[64:65]
	v_add_f32_e32 v16, v16, v17
	global_store_dword v[18:19], v16, off
.LBB0_680:
	s_or_b64 exec, exec, s[6:7]
	v_add_u32_e32 v16, 0xb0, v162
	v_ashrrev_i32_e32 v17, 31, v16
	v_lshlrev_b64 v[18:19], 12, v[16:17]
	v_lshl_add_u64 v[18:19], s[20:21], 0, v[18:19]
	v_lshl_add_u64 v[22:23], v[160:161], 1, v[18:19]
	v_lshlrev_b32_e32 v24, 16, v244
	v_and_b32_e32 v25, 0xffff0000, v244
	v_lshlrev_b32_e32 v18, 16, v245
	v_and_b32_e32 v19, 0xffff0000, v245
	v_lshlrev_b32_e32 v26, 16, v246
	v_and_b32_e32 v27, 0xffff0000, v246
	v_lshlrev_b32_e32 v20, 16, v247
	v_and_b32_e32 v21, 0xffff0000, v247
	v_pk_fma_f32 v[18:19], v[6:7], v[104:105], v[18:19]
	v_pk_fma_f32 v[24:25], v[4:5], v[102:103], v[24:25]
	v_pk_fma_f32 v[20:21], v[2:3], v[100:101], v[20:21]
	v_pk_fma_f32 v[26:27], v[0:1], v[98:99], v[26:27]
	v_cvt_pk_bf16_f32 v0, v24, v25
	v_cvt_pk_bf16_f32 v1, v18, v19
	v_mul_f32_e32 v25, v25, v25
	v_cvt_pk_bf16_f32 v2, v26, v27
	v_cvt_pk_bf16_f32 v3, v20, v21
	v_fmac_f32_e32 v25, v24, v24
	global_store_dwordx4 v[22:23], v[0:3], off
	v_fmac_f32_e32 v25, v18, v18
	v_fmac_f32_e32 v25, v19, v19
	v_fmac_f32_e32 v25, v26, v26
	v_fmac_f32_e32 v25, v27, v27
	v_fmac_f32_e32 v25, v20, v20
	v_fmac_f32_e32 v25, v21, v21
	v_lshlrev_b32_e32 v0, 16, v248
	v_and_b32_e32 v1, 0xffff0000, v248
	v_lshlrev_b32_e32 v2, 16, v249
	v_and_b32_e32 v3, 0xffff0000, v249
	v_lshlrev_b32_e32 v4, 16, v250
	v_and_b32_e32 v5, 0xffff0000, v250
	v_pk_fma_f32 v[12:13], v[12:13], v[84:85], v[0:1]
	v_pk_fma_f32 v[4:5], v[8:9], v[80:81], v[4:5]
	v_mul_f32_e32 v8, v13, v13
	v_pk_fma_f32 v[14:15], v[14:15], v[86:87], v[2:3]
	v_fmac_f32_e32 v8, v12, v12
	v_fmac_f32_e32 v8, v14, v14
	v_fmac_f32_e32 v8, v15, v15
	v_lshlrev_b32_e32 v6, 16, v251
	v_and_b32_e32 v7, 0xffff0000, v251
	v_fmac_f32_e32 v8, v4, v4
	v_pk_fma_f32 v[6:7], v[10:11], v[82:83], v[6:7]
	v_fmac_f32_e32 v8, v5, v5
	v_fmac_f32_e32 v8, v6, v6
	v_cvt_pk_bf16_f32 v0, v12, v13
	v_fmac_f32_e32 v8, v7, v7
	v_cvt_pk_bf16_f32 v1, v14, v15
	v_cvt_pk_bf16_f32 v2, v4, v5
	v_cvt_pk_bf16_f32 v3, v6, v7
	global_store_dwordx4 v[22:23], v[0:3], off offset:256
	s_nop 1
	v_add_f32_e32 v0, v25, v8
	v_mov_b32_e32 v1, v0
	s_nop 1
	v_permlane16_swap_b32_e32 v0, v1
	v_add_f32_e32 v0, v0, v1
	v_mov_b32_e32 v1, v0
	s_nop 1
	v_permlane32_swap_b32_e32 v0, v1
	s_and_saveexec_b64 s[6:7], s[40:41]
	s_cbranch_execz .LBB0_682
	v_lshlrev_b64 v[2:3], 7, v[16:17]
	v_lshl_add_u64 v[2:3], s[22:23], 0, v[2:3]
	v_lshl_add_u64 v[2:3], s[38:39], 2, v[2:3]
	s_lshl_b32 s64, s74, 2
	v_lshl_add_u64 v[2:3], v[2:3], 0, s[64:65]
	v_add_f32_e32 v0, v0, v1
	global_store_dword v[2:3], v0, off
